# v35 + attention loops (DIFF x4, MoBA x2, DSA x1): removed the compiler's conservative s_waitcnt vmcnt(0) before the first ds_read_b64_tr of each tile step (pending LDS-DMA targets other stages; tile a
# baseline (speedup 1.0000x reference)
.LBB0_838:
	s_mulk_i32 s76, 0x6000
	v_add_u32_e32 v192, s76, v175
	v_add_u32_e32 v189, s76, v179
	v_add_u32_e32 v193, s76, v176
	v_add_u32_e32 v191, s76, v177
	v_add_u32_e32 v186, s76, v178
	s_nop 0
	ds_read_b64_tr_b16 v[158:159], v192 offset:8192
	ds_read_b64_tr_b16 v[160:161], v193 offset:8192
	ds_read_b64_tr_b16 v[154:155], v191 offset:8192
	ds_read_b64_tr_b16 v[156:157], v186 offset:8192
	v_add_u32_e32 v187, s76, v180
	v_add_u32_e32 v190, s76, v181
	v_add_u32_e32 v188, s76, v182
	ds_read_b64_tr_b16 v[150:151], v189 offset:8192
	ds_read_b64_tr_b16 v[152:153], v187 offset:8192
	ds_read_b64_tr_b16 v[146:147], v190 offset:8192
	ds_read_b64_tr_b16 v[148:149], v188 offset:8192
	v_cndmask_b32_e64 v194, 0, 1, s[52:53]
	v_cmp_ne_u32_e64 s[34:35], 1, v194
	s_andn2_b64 vcc, exec, s[52:53]
	v_mov_b32_e32 v194, 0xff800000
	s_cbranch_vccnz .LBB0_842
	s_add_i32 s52, s70, 64
	s_cmpk_gt_i32 s52, 0x7f
	s_cbranch_scc1 .LBB0_841
	v_and_b32_e32 v194, 0x3ffffffe, v183
	v_mov_b32_e32 v231, v230
	v_lshl_add_u32 v230, v194, 2, v174
	ds_read2_b64 v[194:197], v230 offset0:112 offset1:113
	ds_read2_b64 v[208:211], v230 offset0:116 offset1:117
	ds_read2_b64 v[212:215], v230 offset0:120 offset1:121
	ds_read2_b64 v[216:219], v230 offset0:124 offset1:125
	ds_read2_b64 v[220:223], v230 offset0:128 offset1:129
	ds_read2_b64 v[224:227], v230 offset0:132 offset1:133
	ds_read2_b64 v[238:241], v230 offset0:136 offset1:137
	ds_read2_b64 v[246:249], v230 offset0:140 offset1:141
	v_mov_b32_e32 v230, v231
	s_waitcnt lgkmcnt(0)
	v_pk_add_f32 v[126:127], v[126:127], v[216:217]
	v_pk_add_f32 v[122:123], v[122:123], v[212:213]
	v_pk_add_f32 v[118:119], v[118:119], v[208:209]
	v_pk_add_f32 v[128:129], v[128:129], v[218:219]
	v_pk_add_f32 v[124:125], v[124:125], v[214:215]
	v_pk_add_f32 v[120:121], v[120:121], v[210:211]
	v_pk_add_f32 v[116:117], v[116:117], v[196:197]
	v_pk_add_f32 v[114:115], v[114:115], v[194:195]
	v_pk_add_f32 v[110:111], v[110:111], v[246:247]
	v_pk_add_f32 v[106:107], v[106:107], v[238:239]
	v_pk_add_f32 v[102:103], v[102:103], v[224:225]
	v_pk_add_f32 v[112:113], v[112:113], v[248:249]
	v_pk_add_f32 v[108:109], v[108:109], v[240:241]
	v_pk_add_f32 v[104:105], v[104:105], v[226:227]
	v_pk_add_f32 v[100:101], v[100:101], v[222:223]
	v_pk_add_f32 v[98:99], v[98:99], v[220:221]

.LBB0_856:
	s_mulk_i32 s71, 0x6000
	v_add_u32_e32 v192, s71, v175
	v_add_u32_e32 v189, s71, v179
	v_add_u32_e32 v193, s71, v176
	v_add_u32_e32 v191, s71, v177
	v_add_u32_e32 v186, s71, v178
	s_nop 0
	ds_read_b64_tr_b16 v[158:159], v192 offset:8192
	ds_read_b64_tr_b16 v[160:161], v193 offset:8192
	ds_read_b64_tr_b16 v[154:155], v191 offset:8192
	ds_read_b64_tr_b16 v[156:157], v186 offset:8192
	v_add_u32_e32 v187, s71, v180
	v_add_u32_e32 v190, s71, v181
	v_add_u32_e32 v188, s71, v182
	ds_read_b64_tr_b16 v[150:151], v189 offset:8192
	ds_read_b64_tr_b16 v[152:153], v187 offset:8192
	ds_read_b64_tr_b16 v[146:147], v190 offset:8192
	ds_read_b64_tr_b16 v[148:149], v188 offset:8192
	v_cndmask_b32_e64 v194, 0, 1, s[52:53]
	v_cmp_ne_u32_e64 s[34:35], 1, v194
	s_andn2_b64 vcc, exec, s[52:53]
	v_mov_b32_e32 v194, 0xff800000
	s_cbranch_vccnz .LBB0_860
	s_cmpk_gt_i32 s70, 0x7f
	s_cbranch_scc1 .LBB0_859
	v_add_u32_e32 v194, 64, v183
	v_and_b32_e32 v194, 0x3ffffffe, v194
	v_mov_b32_e32 v231, v230
	v_lshl_add_u32 v230, v194, 2, v174
	ds_read2_b64 v[194:197], v230 offset0:112 offset1:113
	ds_read2_b64 v[208:211], v230 offset0:116 offset1:117
	ds_read2_b64 v[212:215], v230 offset0:120 offset1:121
	ds_read2_b64 v[216:219], v230 offset0:124 offset1:125
	ds_read2_b64 v[220:223], v230 offset0:128 offset1:129
	ds_read2_b64 v[224:227], v230 offset0:132 offset1:133
	ds_read2_b64 v[238:241], v230 offset0:136 offset1:137
	ds_read2_b64 v[246:249], v230 offset0:140 offset1:141
	v_mov_b32_e32 v230, v231
	s_waitcnt lgkmcnt(0)
	v_pk_add_f32 v[30:31], v[30:31], v[216:217]
	v_pk_add_f32 v[26:27], v[26:27], v[212:213]
	v_pk_add_f32 v[22:23], v[22:23], v[208:209]
	v_pk_add_f32 v[32:33], v[32:33], v[218:219]
	v_pk_add_f32 v[28:29], v[28:29], v[214:215]
	v_pk_add_f32 v[24:25], v[24:25], v[210:211]
	v_pk_add_f32 v[20:21], v[20:21], v[196:197]
	v_pk_add_f32 v[18:19], v[18:19], v[194:195]
	v_pk_add_f32 v[14:15], v[14:15], v[246:247]
	v_pk_add_f32 v[10:11], v[10:11], v[238:239]
	v_pk_add_f32 v[6:7], v[6:7], v[224:225]
	v_pk_add_f32 v[16:17], v[16:17], v[248:249]
	v_pk_add_f32 v[12:13], v[12:13], v[240:241]
	v_pk_add_f32 v[8:9], v[8:9], v[226:227]
	v_pk_add_f32 v[4:5], v[4:5], v[222:223]
	v_pk_add_f32 v[2:3], v[2:3], v[220:221]

.LBB0_883:
	s_mulk_i32 s34, 0x6000
	v_add_u32_e32 v191, s34, v174
	v_add_u32_e32 v188, s34, v178
	v_add_u32_e32 v192, s34, v175
	v_add_u32_e32 v190, s34, v176
	v_add_u32_e32 v185, s34, v177
	s_nop 0
	ds_read_b64_tr_b16 v[158:159], v191 offset:8192
	ds_read_b64_tr_b16 v[160:161], v192 offset:8192
	ds_read_b64_tr_b16 v[154:155], v190 offset:8192
	ds_read_b64_tr_b16 v[156:157], v185 offset:8192
	v_add_u32_e32 v186, s34, v179
	v_add_u32_e32 v189, s34, v180
	v_add_u32_e32 v187, s34, v181
	ds_read_b64_tr_b16 v[150:151], v188 offset:8192
	ds_read_b64_tr_b16 v[152:153], v186 offset:8192
	ds_read_b64_tr_b16 v[146:147], v189 offset:8192
	ds_read_b64_tr_b16 v[148:149], v187 offset:8192
	v_cndmask_b32_e64 v193, 0, 1, s[40:41]
	v_cmp_ne_u32_e64 s[34:35], 1, v193
	s_andn2_b64 vcc, exec, s[40:41]
	v_mov_b32_e32 v193, 0xff800000
	s_cbranch_vccnz .LBB0_887
	s_add_i32 s40, s91, 64
	s_cmpk_gt_i32 s40, 0x7f
	s_cbranch_scc1 .LBB0_886
	v_and_b32_e32 v193, 0x3ffffffe, v182
	v_lshl_add_u32 v193, v193, 2, v173
	ds_read2_b64 v[194:197], v193 offset0:112 offset1:113
	ds_read2_b64 v[208:211], v193 offset0:116 offset1:117
	ds_read2_b64 v[212:215], v193 offset0:120 offset1:121
	ds_read2_b64 v[216:219], v193 offset0:124 offset1:125
	ds_read2_b64 v[220:223], v193 offset0:128 offset1:129
	ds_read2_b64 v[224:227], v193 offset0:132 offset1:133
	ds_read2_b64 v[238:241], v193 offset0:136 offset1:137
	ds_read2_b64 v[246:249], v193 offset0:140 offset1:141
	s_waitcnt lgkmcnt(0)
	v_pk_add_f32 v[126:127], v[126:127], v[216:217]
	v_pk_add_f32 v[122:123], v[122:123], v[212:213]
	v_pk_add_f32 v[118:119], v[118:119], v[208:209]
	v_pk_add_f32 v[128:129], v[128:129], v[218:219]
	v_pk_add_f32 v[124:125], v[124:125], v[214:215]
	v_pk_add_f32 v[120:121], v[120:121], v[210:211]
	v_pk_add_f32 v[116:117], v[116:117], v[196:197]
	v_pk_add_f32 v[114:115], v[114:115], v[194:195]
	v_pk_add_f32 v[110:111], v[110:111], v[246:247]
	v_pk_add_f32 v[106:107], v[106:107], v[238:239]
	v_pk_add_f32 v[102:103], v[102:103], v[224:225]
	v_pk_add_f32 v[112:113], v[112:113], v[248:249]
	v_pk_add_f32 v[108:109], v[108:109], v[240:241]
	v_pk_add_f32 v[104:105], v[104:105], v[226:227]
	v_pk_add_f32 v[100:101], v[100:101], v[222:223]
	v_pk_add_f32 v[98:99], v[98:99], v[220:221]

.LBB0_901:
	s_mulk_i32 s26, 0x6000
	v_add_u32_e32 v191, s26, v174
	v_add_u32_e32 v188, s26, v178
	v_add_u32_e32 v192, s26, v175
	v_add_u32_e32 v190, s26, v176
	v_add_u32_e32 v185, s26, v177
	s_nop 0
	ds_read_b64_tr_b16 v[158:159], v191 offset:8192
	ds_read_b64_tr_b16 v[160:161], v192 offset:8192
	ds_read_b64_tr_b16 v[154:155], v190 offset:8192
	ds_read_b64_tr_b16 v[156:157], v185 offset:8192
	v_add_u32_e32 v186, s26, v179
	v_add_u32_e32 v189, s26, v180
	v_add_u32_e32 v187, s26, v181
	ds_read_b64_tr_b16 v[150:151], v188 offset:8192
	ds_read_b64_tr_b16 v[152:153], v186 offset:8192
	ds_read_b64_tr_b16 v[146:147], v189 offset:8192
	ds_read_b64_tr_b16 v[148:149], v187 offset:8192
	v_cndmask_b32_e64 v193, 0, 1, s[40:41]
	v_cmp_ne_u32_e64 s[34:35], 1, v193
	s_andn2_b64 vcc, exec, s[40:41]
	v_mov_b32_e32 v193, 0xff800000
	s_cbranch_vccnz .LBB0_905
	s_cmpk_gt_i32 s91, 0x7f
	s_cbranch_scc1 .LBB0_904
	v_add_u32_e32 v193, 64, v182
	v_and_b32_e32 v193, 0x3ffffffe, v193
	v_lshl_add_u32 v193, v193, 2, v173
	ds_read2_b64 v[194:197], v193 offset0:112 offset1:113
	ds_read2_b64 v[208:211], v193 offset0:116 offset1:117
	ds_read2_b64 v[212:215], v193 offset0:120 offset1:121
	ds_read2_b64 v[216:219], v193 offset0:124 offset1:125
	ds_read2_b64 v[220:223], v193 offset0:128 offset1:129
	ds_read2_b64 v[224:227], v193 offset0:132 offset1:133
	ds_read2_b64 v[238:241], v193 offset0:136 offset1:137
	ds_read2_b64 v[246:249], v193 offset0:140 offset1:141
	s_waitcnt lgkmcnt(0)
	v_pk_add_f32 v[94:95], v[94:95], v[216:217]
	v_pk_add_f32 v[90:91], v[90:91], v[212:213]
	v_pk_add_f32 v[86:87], v[86:87], v[208:209]
	v_pk_add_f32 v[96:97], v[96:97], v[218:219]
	v_pk_add_f32 v[92:93], v[92:93], v[214:215]
	v_pk_add_f32 v[88:89], v[88:89], v[210:211]
	v_pk_add_f32 v[84:85], v[84:85], v[196:197]
	v_pk_add_f32 v[82:83], v[82:83], v[194:195]
	v_pk_add_f32 v[62:63], v[62:63], v[246:247]
	v_pk_add_f32 v[58:59], v[58:59], v[238:239]
	v_pk_add_f32 v[54:55], v[54:55], v[224:225]
	v_pk_add_f32 v[64:65], v[64:65], v[248:249]
	v_pk_add_f32 v[60:61], v[60:61], v[240:241]
	v_pk_add_f32 v[56:57], v[56:57], v[226:227]
	v_pk_add_f32 v[52:53], v[52:53], v[222:223]
	v_pk_add_f32 v[50:51], v[50:51], v[220:221]

.LBB0_974:
	s_lshl_b32 s34, s72, 14
	v_add_u32_e32 v149, s34, v140
	v_add_u32_e32 v150, s34, v141
	v_add_u32_e32 v147, s34, v142
	v_add_u32_e32 v148, s34, v143
	s_nop 0
	ds_read_b64_tr_b16 v[126:127], v149 offset:8192
	ds_read_b64_tr_b16 v[128:129], v150 offset:8192
	ds_read_b64_tr_b16 v[120:121], v150 offset:10240
	ds_read_b64_tr_b16 v[118:119], v149 offset:10240
	ds_read_b64_tr_b16 v[122:123], v147 offset:8192
	ds_read_b64_tr_b16 v[124:125], v148 offset:8192
	ds_read_b64_tr_b16 v[116:117], v148 offset:10240
	ds_read_b64_tr_b16 v[114:115], v147 offset:10240
	v_cndmask_b32_e64 v151, 0, 1, s[42:43]
	v_cmp_ne_u32_e64 s[34:35], 1, v151
	s_andn2_b64 vcc, exec, s[42:43]
	v_mov_b32_e32 v151, 0xff800000
	s_cbranch_vccnz .LBB0_978
	s_add_i32 s42, s63, 64
	s_cmpk_gt_i32 s42, 0x7f
	s_cbranch_scc1 .LBB0_977
	v_and_b32_e32 v151, 0x3ffffffe, v144
	v_lshl_add_u32 v151, v151, 2, v139
	ds_read2_b64 v[152:155], v151 offset0:112 offset1:113
	ds_read2_b64 v[156:159], v151 offset0:116 offset1:117
	ds_read2_b64 v[162:165], v151 offset0:120 offset1:121
	ds_read2_b64 v[166:169], v151 offset0:124 offset1:125
	ds_read2_b64 v[170:173], v151 offset0:128 offset1:129
	ds_read2_b64 v[174:177], v151 offset0:132 offset1:133
	ds_read2_b64 v[178:181], v151 offset0:136 offset1:137
	ds_read2_b64 v[182:185], v151 offset0:140 offset1:141
	s_waitcnt lgkmcnt(0)
	v_pk_add_f32 v[94:95], v[94:95], v[166:167]
	v_pk_add_f32 v[90:91], v[90:91], v[162:163]
	v_pk_add_f32 v[86:87], v[86:87], v[156:157]
	v_pk_add_f32 v[96:97], v[96:97], v[168:169]
	v_pk_add_f32 v[92:93], v[92:93], v[164:165]
	v_pk_add_f32 v[88:89], v[88:89], v[158:159]
	v_pk_add_f32 v[84:85], v[84:85], v[154:155]
	v_pk_add_f32 v[82:83], v[82:83], v[152:153]
	v_pk_add_f32 v[78:79], v[78:79], v[182:183]
	v_pk_add_f32 v[74:75], v[74:75], v[178:179]
	v_pk_add_f32 v[70:71], v[70:71], v[174:175]
	v_pk_add_f32 v[80:81], v[80:81], v[184:185]
	v_pk_add_f32 v[76:77], v[76:77], v[180:181]
	v_pk_add_f32 v[72:73], v[72:73], v[176:177]
	v_pk_add_f32 v[68:69], v[68:69], v[172:173]
	v_pk_add_f32 v[66:67], v[66:67], v[170:171]

.LBB0_998:
	s_lshl_b32 s34, s65, 14
	v_add_u32_e32 v149, s34, v140
	v_add_u32_e32 v150, s34, v141
	v_add_u32_e32 v147, s34, v142
	v_add_u32_e32 v148, s34, v143
	s_nop 0
	ds_read_b64_tr_b16 v[126:127], v149 offset:8192
	ds_read_b64_tr_b16 v[128:129], v150 offset:8192
	ds_read_b64_tr_b16 v[120:121], v150 offset:10240
	ds_read_b64_tr_b16 v[118:119], v149 offset:10240
	ds_read_b64_tr_b16 v[122:123], v147 offset:8192
	ds_read_b64_tr_b16 v[124:125], v148 offset:8192
	ds_read_b64_tr_b16 v[116:117], v148 offset:10240
	ds_read_b64_tr_b16 v[114:115], v147 offset:10240
	v_cndmask_b32_e64 v151, 0, 1, s[38:39]
	v_cmp_ne_u32_e64 s[34:35], 1, v151
	s_andn2_b64 vcc, exec, s[38:39]
	v_mov_b32_e32 v151, 0xff800000
	s_cbranch_vccnz .LBB0_1002
	s_cmpk_gt_i32 s63, 0x7f
	s_cbranch_scc1 .LBB0_1001
	v_add_u32_e32 v151, 64, v144
	v_and_b32_e32 v151, 0x3ffffffe, v151
	v_lshl_add_u32 v151, v151, 2, v139
	ds_read2_b64 v[152:155], v151 offset0:112 offset1:113
	ds_read2_b64 v[156:159], v151 offset0:116 offset1:117
	ds_read2_b64 v[162:165], v151 offset0:120 offset1:121
	ds_read2_b64 v[166:169], v151 offset0:124 offset1:125
	ds_read2_b64 v[170:173], v151 offset0:128 offset1:129
	ds_read2_b64 v[174:177], v151 offset0:132 offset1:133
	ds_read2_b64 v[178:181], v151 offset0:136 offset1:137
	ds_read2_b64 v[182:185], v151 offset0:140 offset1:141
	s_waitcnt lgkmcnt(0)
	v_pk_add_f32 v[30:31], v[30:31], v[166:167]
	v_pk_add_f32 v[26:27], v[26:27], v[162:163]
	v_pk_add_f32 v[22:23], v[22:23], v[156:157]
	v_pk_add_f32 v[32:33], v[32:33], v[168:169]
	v_pk_add_f32 v[28:29], v[28:29], v[164:165]
	v_pk_add_f32 v[24:25], v[24:25], v[158:159]
	v_pk_add_f32 v[20:21], v[20:21], v[154:155]
	v_pk_add_f32 v[18:19], v[18:19], v[152:153]
	v_pk_add_f32 v[14:15], v[14:15], v[182:183]
	v_pk_add_f32 v[10:11], v[10:11], v[178:179]
	v_pk_add_f32 v[6:7], v[6:7], v[174:175]
	v_pk_add_f32 v[16:17], v[16:17], v[184:185]
	v_pk_add_f32 v[12:13], v[12:13], v[180:181]
	v_pk_add_f32 v[8:9], v[8:9], v[176:177]
	v_pk_add_f32 v[4:5], v[4:5], v[172:173]
	v_pk_add_f32 v[2:3], v[2:3], v[170:171]

; #define LAS __attribute__((address_space(3)))
; template <int DQK, int DV, int MODE, int S> ...
;     ...
;         if (k0 <= qpos0 + 31) {
;             const LAS unsigned char* sb = lds + st * L::STG;
;             f32x16 p0, p1;
;             if (MODE == 2) {
;                 const unsigned nw = ~*(const LAS unsigned*)(lds + L::MASKOFF + (wave * S + st) * 256 + lane * 4);
; #pragma unroll
;                 for (int r = 0; r < 16; ++r) { p0[r] = __uint_as_float((unsigned)__builtin_amdgcn_sbfe((int)nw, r, 1) & 0xff800000u); p1[r] = __uint_as_float((unsigned)__builtin_amdgcn_sbfe((int)nw, 16 + r, 1) & 0xff800000u); }
;             } else if (MODE == 1) {
;                 const int n = kt >> 2; const float cv = (n == jblk || ((selb >> n) & 1u)) ? 0.f : -INFINITY;
; #pragma unroll
;                 for (int r = 0; r < 16; ++r) { p0[r] = cv; p1[r] = cv; }
;             } else {
; #pragma unroll
;                 for (int r = 0; r < 16; ++r) { p0[r] = 0.f; p1[r] = 0.f; }
;             }
; #pragma unroll
;             for (int db = 0; db < DQK / 64; ++db) {
;                 f16x8 kf0[4], kf1[4];
; #pragma unroll
;                 for (int d = 0; d < 4; ++d) { kf0[d] = *(const LAS f16x8*)(sb + koff[4 * db + d]); kf1[d] = *(const LAS f16x8*)(sb + koff[4 * db + d] + 32 * L::CPRK * 16); }
;                 __builtin_amdgcn_sched_barrier(0);
; #pragma unroll
;                 for (int d = 0; d < 4; ++d) {
;                     p0 = __builtin_amdgcn_mfma_f32_32x32x16_f16(kf0[d], qf[4 * db + d], p0, 0, 0, 0);
;                     p1 = __builtin_amdgcn_mfma_f32_32x32x16_f16(kf1[d], qf[4 * db + d], p1, 0, 0, 0); }
;                 __builtin_amdgcn_sched_barrier(0);
;             }
;             f16x8 vfa[NB_], vfb[NB_];
;             FA_VREADD(vfa, 0);
;             __builtin_amdgcn_sched_barrier(0);
;             if (qpos0 - (k0 + 63) < 128) {
.LBB0_1042:
	s_cmp_gt_u32 s42, s40
	s_cbranch_scc1 .LBB0_1035
	v_lshl_add_u32 v0, v146, 2, s4
	v_lshl_add_u32 v0, s44, 8, v0
	ds_read_b32 v0, v0
	s_lshl_b32 s36, s44, 14
	v_add3_u32 v82, s36, v157, v156
	ds_read_b128 v[130:133], v82
	ds_read_b128 v[134:137], v82 offset:8192
	v_add3_u32 v82, s36, v158, v156
	s_waitcnt lgkmcnt(0)
	v_and_b32_e32 v66, 0x20000, v0
	v_and_b32_e32 v68, 0x10000, v0
	v_cmp_eq_u32_e32 vcc, 0, v66
	v_and_b32_e32 v70, 0x40000, v0
	v_and_b32_e32 v72, 0x100000, v0
	v_cndmask_b32_e32 v67, 0, v233, vcc
	v_cmp_eq_u32_e32 vcc, 0, v68
	v_and_b32_e32 v68, 0x80000, v0
	v_and_b32_e32 v74, 0x400000, v0
	v_cndmask_b32_e32 v66, 0, v233, vcc
	v_cmp_eq_u32_e32 vcc, 0, v68
	v_and_b32_e32 v76, 0x1000000, v0
	v_and_b32_e32 v78, 0x4000000, v0
	v_cndmask_b32_e32 v69, 0, v233, vcc
	v_cmp_eq_u32_e32 vcc, 0, v70
	v_and_b32_e32 v70, 0x200000, v0
	v_and_b32_e32 v80, 0x10000000, v0
	v_cndmask_b32_e32 v68, 0, v233, vcc
	v_cmp_eq_u32_e32 vcc, 0, v70
	v_and_b32_e32 v81, 0x8000, v0
	ds_read_b128 v[138:141], v82
	ds_read_b128 v[142:145], v82 offset:8192
	v_cndmask_b32_e32 v71, 0, v233, vcc
	v_cmp_eq_u32_e32 vcc, 0, v72
	v_and_b32_e32 v72, 0x800000, v0
	v_add3_u32 v82, s36, v159, v156
	v_cndmask_b32_e32 v70, 0, v233, vcc
	v_cmp_eq_u32_e32 vcc, 0, v72
	ds_read_b128 v[180:183], v82
	ds_read_b128 v[184:187], v82 offset:8192
	v_cndmask_b32_e32 v73, 0, v233, vcc
	v_cmp_eq_u32_e32 vcc, 0, v74
	v_and_b32_e32 v74, 0x2000000, v0
	v_add3_u32 v82, s36, v160, v156
	v_cndmask_b32_e32 v72, 0, v233, vcc
	v_cmp_eq_u32_e32 vcc, 0, v74
	ds_read_b128 v[188:191], v82
	ds_read_b128 v[192:195], v82 offset:8192
	v_cndmask_b32_e32 v75, 0, v233, vcc
	v_cmp_eq_u32_e32 vcc, 0, v76
	v_and_b32_e32 v76, 0x8000000, v0
	s_nop 0
	v_cndmask_b32_e32 v74, 0, v233, vcc
	v_cmp_eq_u32_e32 vcc, 0, v76
	s_nop 1
	v_cndmask_b32_e32 v77, 0, v233, vcc
	v_cmp_eq_u32_e32 vcc, 0, v78
	v_and_b32_e32 v78, 0x20000000, v0
	s_nop 0
	v_cndmask_b32_e32 v76, 0, v233, vcc
	v_cmp_eq_u32_e32 vcc, 0, v78
	s_nop 1
	v_cndmask_b32_e32 v79, 0, v233, vcc
	v_cmp_eq_u32_e32 vcc, 0, v80
	v_and_b32_e32 v80, 2.0, v0
	s_nop 0
	v_cndmask_b32_e32 v78, 0, v233, vcc
	v_cmp_eq_u32_e32 vcc, 0, v80
	s_nop 1
	v_cndmask_b32_e32 v80, 0, v233, vcc
	v_cmp_ne_u32_e32 vcc, 0, v81
	v_and_b32_e32 v81, 0x4000, v0
	s_nop 0
	v_cndmask_b32_e64 v97, v233, 0, vcc
	v_cmp_ne_u32_e32 vcc, 0, v81
	v_and_b32_e32 v81, 0x2000, v0
	s_nop 0
	v_cndmask_b32_e64 v96, v233, 0, vcc
	v_cmp_ne_u32_e32 vcc, 0, v81
	v_and_b32_e32 v81, 0x1000, v0
	s_nop 0
	v_cndmask_b32_e64 v95, v233, 0, vcc
	v_cmp_ne_u32_e32 vcc, 0, v81
	v_and_b32_e32 v81, 0x800, v0
	s_nop 0
	v_cndmask_b32_e64 v94, v233, 0, vcc
	v_cmp_ne_u32_e32 vcc, 0, v81
	v_and_b32_e32 v81, 0x400, v0
	s_nop 0
	v_cndmask_b32_e64 v93, v233, 0, vcc
	v_cmp_ne_u32_e32 vcc, 0, v81
	v_and_b32_e32 v81, 0x200, v0
	s_nop 0
	v_cndmask_b32_e64 v92, v233, 0, vcc
	v_cmp_ne_u32_e32 vcc, 0, v81
	v_and_b32_e32 v81, 0x100, v0
	s_nop 0
	v_cndmask_b32_e64 v91, v233, 0, vcc
	v_cmp_ne_u32_e32 vcc, 0, v81
	v_and_b32_e32 v81, 0x80, v0
	s_nop 0
	v_cndmask_b32_e64 v90, v233, 0, vcc
	v_cmp_ne_u32_e32 vcc, 0, v81
	v_and_b32_e32 v81, 64, v0
	s_nop 0
	v_cndmask_b32_e64 v89, v233, 0, vcc
	v_cmp_ne_u32_e32 vcc, 0, v81
	v_and_b32_e32 v81, 32, v0
	s_nop 0
	v_cndmask_b32_e64 v88, v233, 0, vcc
	v_cmp_ne_u32_e32 vcc, 0, v81
	v_and_b32_e32 v81, 16, v0
	s_nop 0
	v_cndmask_b32_e64 v87, v233, 0, vcc
	v_cmp_ne_u32_e32 vcc, 0, v81
	v_and_b32_e32 v81, 8, v0
	s_nop 0
	v_cndmask_b32_e64 v86, v233, 0, vcc
	v_cmp_ne_u32_e32 vcc, 0, v81
	v_and_b32_e32 v81, 4, v0
	s_nop 0
	v_cndmask_b32_e64 v85, v233, 0, vcc
	v_cmp_ne_u32_e32 vcc, 0, v81
	v_and_b32_e32 v81, 2, v0
	s_nop 0
	v_cndmask_b32_e64 v84, v233, 0, vcc
	v_cmp_ne_u32_e32 vcc, 0, v81
	v_and_b32_e32 v81, 1, v0
	s_nop 0
	v_cndmask_b32_e64 v83, v233, 0, vcc
	v_cmp_eq_u32_e32 vcc, 1, v81
	s_nop 1
	v_cndmask_b32_e64 v82, v233, 0, vcc
	v_cmp_gt_i32_e32 vcc, 0, v0
	s_nop 1
	v_cndmask_b32_e64 v81, v233, 0, vcc
	v_mfma_f32_32x32x16_f16 v[82:97], v[130:133], v[122:125], v[82:97]
	s_nop 0
	v_mfma_f32_32x32x16_f16 v[66:81], v[134:137], v[122:125], v[66:81]
	s_waitcnt lgkmcnt(0)
	v_mfma_f32_32x32x16_f16 v[82:97], v[138:141], v[98:101], v[82:97]
	v_mfma_f32_32x32x16_f16 v[66:81], v[142:145], v[98:101], v[66:81]
	v_mfma_f32_32x32x16_f16 v[82:97], v[180:183], v[102:105], v[82:97]
	v_mfma_f32_32x32x16_f16 v[66:81], v[184:187], v[102:105], v[66:81]
	v_mfma_f32_32x32x16_f16 v[82:97], v[188:191], v[106:109], v[82:97]
	v_mfma_f32_32x32x16_f16 v[66:81], v[192:195], v[106:109], v[66:81]
	v_add3_u32 v0, s36, v161, v156
	ds_read_b128 v[130:133], v0
	ds_read_b128 v[134:137], v0 offset:8192
	v_add3_u32 v0, s36, v162, v156
	ds_read_b128 v[138:141], v0
	ds_read_b128 v[142:145], v0 offset:8192
	v_add3_u32 v0, s36, v163, v156
	ds_read_b128 v[180:183], v0
	ds_read_b128 v[184:187], v0 offset:8192
	v_add3_u32 v0, s36, v164, v156
	ds_read_b128 v[188:191], v0
	ds_read_b128 v[192:195], v0 offset:8192
	s_waitcnt lgkmcnt(0)
	v_mfma_f32_32x32x16_f16 v[82:97], v[130:133], v[110:113], v[82:97]
	v_add3_u32 v130, s36, v166, v165
	v_add_u32_e32 v0, v130, v167
	v_add3_u32 v131, s36, v171, v165
	v_add_u32_e32 v179, v131, v172
	v_mfma_f32_32x32x16_f16 v[66:81], v[134:137], v[110:113], v[66:81]
	v_mfma_f32_32x32x16_f16 v[82:97], v[138:141], v[114:117], v[82:97]
	v_mfma_f32_32x32x16_f16 v[66:81], v[142:145], v[114:117], v[66:81]
	v_mfma_f32_32x32x16_f16 v[82:97], v[180:183], v[118:121], v[82:97]
	v_add_u32_e32 v182, v130, v169
	v_add_u32_e32 v180, v130, v168
	v_add_u32_e32 v181, v131, v173
	s_nop 0
	ds_read_b64_tr_b16 v[138:139], v0
	ds_read_b64_tr_b16 v[140:141], v179
	ds_read_b64_tr_b16 v[134:135], v180
	ds_read_b64_tr_b16 v[136:137], v181
	v_add_u32_e32 v183, v131, v174
	v_mfma_f32_32x32x16_f16 v[66:81], v[184:187], v[118:121], v[66:81]
	v_add_u32_e32 v184, v130, v170
	v_add_u32_e32 v185, v131, v175
	ds_read_b64_tr_b16 v[142:143], v182
	ds_read_b64_tr_b16 v[144:145], v183
	ds_read_b64_tr_b16 v[130:131], v184
	ds_read_b64_tr_b16 v[132:133], v185
	v_mfma_f32_32x32x16_f16 v[82:97], v[188:191], v[126:129], v[82:97]
	v_mfma_f32_32x32x16_f16 v[66:81], v[192:195], v[126:129], v[66:81]
	s_cmpk_gt_i32 s41, 0x7f
	s_cbranch_scc1 .LBB0_1045
; #define LAS __attribute__((address_space(3)))
; template <int DQK, int DV, int MODE, int S> ...
;     ...
;             if (qpos0 - (k0 + 63) < 128) {
;                 const int j0 = 224 - (qpos0 + r32 - k0 - 4 * hi), sf = j0 & 1; const LAS float* rp = tab + sf * TAB2 + (j0 - sf);
; #pragma unroll
;                 for (int g = 0; g < 4; ++g) { const f32x2 x0 = *(const LAS f32x2*)(rp + 8 * g), x1 = *(const LAS f32x2*)(rp + 8 * g + 2), y0 = *(const LAS f32x2*)(rp + 32 + 8 * g), y1 = *(const LAS f32x2*)(rp + 34 + 8 * g);
;                     p0[4 * g] += x0.x; p0[4 * g + 1] += x0.y; p0[4 * g + 2] += x1.x; p0[4 * g + 3] += x1.y; p1[4 * g] += y0.x; p1[4 * g + 1] += y0.y; p1[4 * g + 2] += y1.x; p1[4 * g + 3] += y1.y; }
	v_add_u32_e32 v186, s42, v177
	v_and_b32_e32 v186, 0x3ffffffe, v186
	v_lshl_add_u32 v224, v186, 2, v176
	ds_read2_b64 v[186:189], v224 offset0:112 offset1:113
	ds_read2_b64 v[190:193], v224 offset0:116 offset1:117
	ds_read2_b64 v[194:197], v224 offset0:120 offset1:121
	ds_read2_b64 v[208:211], v224 offset0:124 offset1:125
	ds_read2_b64 v[212:215], v224 offset0:128 offset1:129
	ds_read2_b64 v[216:219], v224 offset0:132 offset1:133
	ds_read2_b64 v[220:223], v224 offset0:136 offset1:137
	ds_read2_b64 v[224:227], v224 offset0:140 offset1:141
	s_waitcnt lgkmcnt(4)
	v_pk_add_f32 v[94:95], v[94:95], v[208:209]
	v_pk_add_f32 v[90:91], v[90:91], v[194:195]
	v_pk_add_f32 v[86:87], v[86:87], v[190:191]
	v_pk_add_f32 v[96:97], v[96:97], v[210:211]
	v_pk_add_f32 v[92:93], v[92:93], v[196:197]
	v_pk_add_f32 v[88:89], v[88:89], v[192:193]
	v_pk_add_f32 v[84:85], v[84:85], v[188:189]
	v_pk_add_f32 v[82:83], v[82:83], v[186:187]
	s_waitcnt lgkmcnt(0)
	v_pk_add_f32 v[78:79], v[78:79], v[224:225]
	v_pk_add_f32 v[74:75], v[74:75], v[220:221]
	v_pk_add_f32 v[70:71], v[70:71], v[216:217]
	v_pk_add_f32 v[80:81], v[80:81], v[226:227]
	v_pk_add_f32 v[76:77], v[76:77], v[222:223]
	v_pk_add_f32 v[72:73], v[72:73], v[218:219]
	v_pk_add_f32 v[68:69], v[68:69], v[214:215]
	v_pk_add_f32 v[66:67], v[66:67], v[212:213]
